# bf16-source norm phases (P7,P18): next row's loads issued one row ahead with a counted vmcnt(4) at the loop top; on top of v062
# baseline (speedup 1.0000x reference)
.LBB0_556:
	s_ashr_i32 s7, s6, 31
	s_lshl_b64 s[0:1], s[6:7], 12
	s_ashr_i32 s7, s11, 7
	s_mul_hi_i32 s8, s7, 0xc000
	s_mul_i32 s7, s7, 0xc000
	s_add_u32 s7, s3, s7
	s_addc_u32 s13, s59, s8
	s_add_u32 s8, s7, 0x6000
	s_addc_u32 s9, s13, 0
	s_add_u32 s12, s7, 0x8000
	s_addc_u32 s13, s13, 0
	v_lshlrev_b32_e32 v38, 2, v104
	global_load_dwordx4 v[72:75], v38, s[12:13]
	global_load_dwordx4 v[76:79], v38, s[12:13] offset:16
	global_load_dwordx4 v[80:83], v106, s[12:13]
	global_load_dwordx4 v[84:87], v106, s[12:13] offset:16
	global_load_dwordx4 v[92:95], v1, s[12:13] offset:16
	global_load_dwordx4 v[88:91], v1, s[12:13]
	global_load_dwordx4 v[34:37], v38, s[8:9]
	s_nop 0
	global_load_dwordx4 v[38:41], v38, s[8:9] offset:16
	s_nop 0
	global_load_dwordx4 v[100:103], v105, s[12:13] offset:16
	global_load_dwordx4 v[96:99], v105, s[12:13]
	global_load_dwordx4 v[42:45], v106, s[8:9]
	global_load_dwordx4 v[46:49], v106, s[8:9] offset:16
	global_load_dwordx4 v[50:53], v1, s[8:9]
	global_load_dwordx4 v[54:57], v1, s[8:9] offset:16
	global_load_dwordx4 v[58:61], v105, s[8:9]
	global_load_dwordx4 v[62:65], v105, s[8:9] offset:16
	v_lshl_add_u64 v[70:71], v[68:69], 0, s[0:1]
	s_mov_b64 s[8:9], 0
	s_waitcnt vmcnt(0)
	v_pk_add_f32 v[72:73], v[72:73], 1.0 op_sel_hi:[1,0]
	v_pk_add_f32 v[74:75], v[74:75], 1.0 op_sel_hi:[1,0]
	v_pk_add_f32 v[76:77], v[76:77], 1.0 op_sel_hi:[1,0]
	v_pk_add_f32 v[78:79], v[78:79], 1.0 op_sel_hi:[1,0]
	v_pk_add_f32 v[80:81], v[80:81], 1.0 op_sel_hi:[1,0]
	v_pk_add_f32 v[82:83], v[82:83], 1.0 op_sel_hi:[1,0]
	v_pk_add_f32 v[84:85], v[84:85], 1.0 op_sel_hi:[1,0]
	v_pk_add_f32 v[86:87], v[86:87], 1.0 op_sel_hi:[1,0]
	v_pk_add_f32 v[88:89], v[88:89], 1.0 op_sel_hi:[1,0]
	v_pk_add_f32 v[90:91], v[90:91], 1.0 op_sel_hi:[1,0]
	v_pk_add_f32 v[92:93], v[92:93], 1.0 op_sel_hi:[1,0]
	v_pk_add_f32 v[94:95], v[94:95], 1.0 op_sel_hi:[1,0]
	v_pk_add_f32 v[96:97], v[96:97], 1.0 op_sel_hi:[1,0]
	v_pk_add_f32 v[98:99], v[98:99], 1.0 op_sel_hi:[1,0]
	v_pk_add_f32 v[100:101], v[100:101], 1.0 op_sel_hi:[1,0]
	v_pk_add_f32 v[102:103], v[102:103], 1.0 op_sel_hi:[1,0]
	v_lshl_add_u64 v[246:247], v[70:71], 0, s[8:9]
	v_add_co_u32_e32 v246, vcc, 0x16400000, v246
	s_nop 1
	v_addc_co_u32_e32 v247, vcc, 0, v247, vcc
	global_load_dwordx4 v[230:233], v[246:247], off offset:3072
	global_load_dwordx4 v[234:237], v[246:247], off
	global_load_dwordx4 v[238:241], v[246:247], off offset:1024
	global_load_dwordx4 v[242:245], v[246:247], off offset:2048
	s_waitcnt vmcnt(0)
	s_branch .Lnbody_LBB0_557
.LBB0_557:
	s_waitcnt vmcnt(4)
.Lnbody_LBB0_557:
	v_lshl_add_u64 v[114:115], v[70:71], 0, s[8:9]
	v_add_co_u32_e32 v126, vcc, 0x16400000, v114
	v_add_co_u32_e64 v130, s[0:1], s10, v114
	s_nop 0
	v_addc_co_u32_e32 v127, vcc, 0, v115, vcc
	v_addc_co_u32_e64 v131, s[0:1], 0, v115, s[0:1]
	s_nop 0
	s_add_u32 s8, s8, 0x1000
	s_addc_u32 s9, s9, 0
	s_cmp_eq_u32 s8, 0x10000
	v_mov_b64_e32 v[114:115], v[230:231]
	v_mov_b64_e32 v[116:117], v[232:233]
	v_mov_b64_e32 v[118:119], v[234:235]
	v_mov_b64_e32 v[120:121], v[236:237]
	v_mov_b64_e32 v[122:123], v[238:239]
	v_mov_b64_e32 v[124:125], v[240:241]
	v_mov_b64_e32 v[126:127], v[242:243]
	v_mov_b64_e32 v[128:129], v[244:245]
	s_cbranch_scc1 .Lnpf_LBB0_557
	v_lshl_add_u64 v[246:247], v[70:71], 0, s[8:9]
	v_add_co_u32_e32 v246, vcc, 0x16400000, v246
	s_nop 1
	v_addc_co_u32_e32 v247, vcc, 0, v247, vcc
	global_load_dwordx4 v[230:233], v[246:247], off offset:3072
	global_load_dwordx4 v[234:237], v[246:247], off
	global_load_dwordx4 v[238:241], v[246:247], off offset:1024
	global_load_dwordx4 v[242:245], v[246:247], off offset:2048
.Lnpf_LBB0_557:
	v_and_b32_e32 v135, 0xffff0000, v114
	v_and_b32_e32 v134, 0xffff0000, v116
	v_lshlrev_b32_e32 v138, 16, v120
	v_and_b32_e32 v139, 0xffff0000, v120
	v_lshlrev_b32_e32 v140, 16, v118
	v_and_b32_e32 v141, 0xffff0000, v118
	v_lshlrev_b32_e32 v133, 16, v114
	v_lshlrev_b32_e32 v132, 16, v116
	v_lshlrev_b32_e32 v136, 16, v117
	v_and_b32_e32 v114, 0xffff0000, v117
	v_lshlrev_b32_e32 v116, 16, v121
	v_and_b32_e32 v117, 0xffff0000, v121
	v_lshlrev_b32_e32 v120, 16, v119
	v_and_b32_e32 v121, 0xffff0000, v119
	v_lshlrev_b32_e32 v118, 16, v125
	v_and_b32_e32 v119, 0xffff0000, v125
	v_lshlrev_b32_e32 v142, 16, v124
	v_and_b32_e32 v143, 0xffff0000, v124
	v_lshlrev_b32_e32 v124, 16, v123
	v_and_b32_e32 v125, 0xffff0000, v123
	v_lshlrev_b32_e32 v144, 16, v122
	v_and_b32_e32 v145, 0xffff0000, v122
	v_lshlrev_b32_e32 v122, 16, v129
	v_and_b32_e32 v123, 0xffff0000, v129
	v_lshlrev_b32_e32 v146, 16, v128
	v_and_b32_e32 v147, 0xffff0000, v128
	v_lshlrev_b32_e32 v128, 16, v127
	v_and_b32_e32 v129, 0xffff0000, v127
	v_lshlrev_b32_e32 v148, 16, v126
	v_and_b32_e32 v149, 0xffff0000, v126
	v_pk_mul_f32 v[126:127], v[134:135], v[134:135]
	v_pk_mul_f32 v[152:153], v[138:139], v[138:139]
	v_pk_mul_f32 v[156:157], v[140:141], v[140:141]
	v_lshlrev_b32_e32 v137, 16, v115
	v_pk_mul_f32 v[150:151], v[116:117], v[116:117]
	v_pk_mul_f32 v[154:155], v[120:121], v[120:121]
	v_pk_mul_f32 v[164:165], v[144:145], v[144:145]
	v_mov_b32_e32 v175, v135
	v_pk_fma_f32 v[126:127], v[132:133], v[132:133], v[126:127]
	v_add_f32_e32 v113, v152, v153
	v_add_f32_e32 v135, v156, v157
	v_and_b32_e32 v115, 0xffff0000, v115
	v_pk_mul_f32 v[160:161], v[142:143], v[142:143]
	v_pk_mul_f32 v[162:163], v[124:125], v[124:125]
	v_mov_b32_e32 v174, v133
	v_add_f32_e32 v152, v164, v165
	v_mov_b32_e32 v133, v134
	v_pk_fma_f32 v[126:127], v[136:137], v[136:137], v[126:127]
	v_add_f32_e32 v113, v150, v113
	v_add_f32_e32 v134, v154, v135
	v_pk_mul_f32 v[158:159], v[118:119], v[118:119]
	v_pk_mul_f32 v[172:173], v[148:149], v[148:149]
	v_mov_b32_e32 v176, v137
	v_mov_b32_e32 v177, v115
	v_add_f32_e32 v153, v160, v161
	v_add_f32_e32 v135, v162, v152
	v_mov_b32_e32 v137, v114
	v_pk_fma_f32 v[114:115], v[114:115], v[114:115], v[126:127]
	v_add_f32_e32 v113, v151, v113
	v_add_f32_e32 v126, v155, v134
	v_pk_mul_f32 v[168:169], v[146:147], v[146:147]
	v_pk_mul_f32 v[170:171], v[128:129], v[128:129]
	v_add_f32_e32 v156, v172, v173
	v_add_f32_e32 v150, v158, v153
	v_add_f32_e32 v127, v163, v135
	v_add_f32_e32 v113, v126, v113
	v_pk_mul_f32 v[166:167], v[122:123], v[122:123]
	v_add_f32_e32 v157, v168, v169
	v_add_f32_e32 v152, v170, v156
	v_add_f32_e32 v134, v159, v150
	v_add_f32_e32 v113, v113, v127
	v_add_f32_e32 v153, v166, v157
	v_add_f32_e32 v135, v171, v152
	v_add_f32_e32 v113, v134, v113
	v_add_f32_e32 v150, v167, v153
	v_add_f32_e32 v113, v135, v113
	v_add_f32_e32 v113, v150, v113
	v_add_f32_e32 v113, v115, v113
	v_add_f32_e32 v113, v114, v113
	ds_bpermute_b32 v114, v107, v113
	s_waitcnt lgkmcnt(0)
	v_add_f32_e32 v113, v113, v114
	ds_bpermute_b32 v114, v108, v113
	s_waitcnt lgkmcnt(0)
	v_add_f32_e32 v113, v113, v114
	ds_bpermute_b32 v114, v109, v113
	s_waitcnt lgkmcnt(0)
	v_add_f32_e32 v113, v113, v114
	ds_bpermute_b32 v114, v110, v113
	s_waitcnt lgkmcnt(0)
	v_add_f32_e32 v113, v113, v114
	ds_bpermute_b32 v114, v111, v113
	s_waitcnt lgkmcnt(0)
	v_add_f32_e32 v113, v113, v114
	ds_bpermute_b32 v114, v112, v113
	s_waitcnt lgkmcnt(0)
	v_add_f32_e32 v113, v113, v114
	v_fmamk_f32 v113, v113, 0x3a000000, v67
	v_rsq_f32_e32 v114, v113
	s_nop 0
	v_pk_mul_f32 v[126:127], v[114:115], v[140:141] op_sel_hi:[0,1]
	v_pk_mul_f32 v[120:121], v[114:115], v[120:121] op_sel_hi:[0,1]
	v_pk_mul_f32 v[134:135], v[114:115], v[138:139] op_sel_hi:[0,1]
	v_pk_mul_f32 v[116:117], v[114:115], v[116:117] op_sel_hi:[0,1]
	v_pk_mul_f32 v[138:139], v[114:115], v[144:145] op_sel_hi:[0,1]
	v_pk_mul_f32 v[124:125], v[114:115], v[124:125] op_sel_hi:[0,1]
	v_pk_mul_f32 v[140:141], v[114:115], v[142:143] op_sel_hi:[0,1]
	v_pk_mul_f32 v[118:119], v[114:115], v[118:119] op_sel_hi:[0,1]
	v_pk_mul_f32 v[142:143], v[114:115], v[148:149] op_sel_hi:[0,1]
	v_pk_mul_f32 v[128:129], v[114:115], v[128:129] op_sel_hi:[0,1]
	v_pk_mul_f32 v[144:145], v[114:115], v[146:147] op_sel_hi:[0,1]
	v_pk_mul_f32 v[122:123], v[114:115], v[122:123] op_sel_hi:[0,1]
	v_pk_mul_f32 v[146:147], v[114:115], v[174:175] op_sel_hi:[0,1]
	v_pk_mul_f32 v[148:149], v[114:115], v[176:177] op_sel_hi:[0,1]
	v_pk_mul_f32 v[132:133], v[114:115], v[132:133] op_sel_hi:[0,1]
	v_pk_mul_f32 v[114:115], v[114:115], v[136:137] op_sel_hi:[0,1]
	v_pk_mul_f32 v[126:127], v[6:7], v[126:127]
	v_pk_mul_f32 v[120:121], v[8:9], v[120:121]
	v_pk_mul_f32 v[134:135], v[2:3], v[134:135]
	v_pk_mul_f32 v[116:117], v[4:5], v[116:117]
	v_pk_mul_f32 v[136:137], v[14:15], v[138:139]
	v_pk_mul_f32 v[124:125], v[16:17], v[124:125]
	v_pk_mul_f32 v[138:139], v[10:11], v[140:141]
	v_pk_mul_f32 v[118:119], v[12:13], v[118:119]
	v_pk_mul_f32 v[140:141], v[22:23], v[142:143]
	v_pk_mul_f32 v[128:129], v[24:25], v[128:129]
	v_pk_mul_f32 v[142:143], v[18:19], v[144:145]
	v_pk_mul_f32 v[122:123], v[20:21], v[122:123]
	v_pk_mul_f32 v[144:145], v[30:31], v[146:147]
	v_pk_mul_f32 v[146:147], v[32:33], v[148:149]
	v_pk_mul_f32 v[132:133], v[26:27], v[132:133]
	v_pk_mul_f32 v[114:115], v[28:29], v[114:115]
	v_pk_fma_f32 v[126:127], v[72:73], v[126:127], v[34:35]
	v_pk_fma_f32 v[120:121], v[74:75], v[120:121], v[36:37]
	v_pk_fma_f32 v[134:135], v[76:77], v[134:135], v[38:39]
	v_pk_fma_f32 v[148:149], v[78:79], v[116:117], v[40:41]
	v_pk_fma_f32 v[136:137], v[80:81], v[136:137], v[42:43]
	v_pk_fma_f32 v[124:125], v[82:83], v[124:125], v[44:45]
	v_pk_fma_f32 v[138:139], v[84:85], v[138:139], v[46:47]
	v_pk_fma_f32 v[150:151], v[86:87], v[118:119], v[48:49]
	v_pk_fma_f32 v[140:141], v[88:89], v[140:141], v[50:51]
	v_pk_fma_f32 v[128:129], v[90:91], v[128:129], v[52:53]
	v_pk_fma_f32 v[142:143], v[92:93], v[142:143], v[54:55]
	v_pk_fma_f32 v[152:153], v[94:95], v[122:123], v[56:57]
	v_pk_fma_f32 v[144:145], v[96:97], v[144:145], v[58:59]
	v_pk_fma_f32 v[146:147], v[98:99], v[146:147], v[60:61]
	v_pk_fma_f32 v[132:133], v[100:101], v[132:133], v[62:63]
	v_pk_fma_f32 v[154:155], v[102:103], v[114:115], v[64:65]
	v_cvt_pk_bf16_f32 v114, v126, v127
	v_cvt_pk_bf16_f32 v115, v120, v121
	v_cvt_pk_bf16_f32 v116, v134, v135
	v_cvt_pk_bf16_f32 v117, v148, v149
	v_cvt_pk_bf16_f32 v118, v136, v137
	v_cvt_pk_bf16_f32 v119, v124, v125
	v_cvt_pk_bf16_f32 v120, v138, v139
	v_cvt_pk_bf16_f32 v121, v150, v151
	v_cvt_pk_bf16_f32 v122, v140, v141
	v_cvt_pk_bf16_f32 v123, v128, v129
	v_cvt_pk_bf16_f32 v124, v142, v143
	v_cvt_pk_bf16_f32 v125, v152, v153
	v_cvt_pk_bf16_f32 v126, v144, v145
	v_cvt_pk_bf16_f32 v127, v146, v147
	v_cvt_pk_bf16_f32 v128, v132, v133
	v_cvt_pk_bf16_f32 v129, v154, v155
	global_store_dwordx4 v[130:131], v[114:117], off
	global_store_dwordx4 v[130:131], v[118:121], off offset:1024
	global_store_dwordx4 v[130:131], v[122:125], off offset:2048
	global_store_dwordx4 v[130:131], v[126:129], off offset:3072
	s_cbranch_scc0 .LBB0_557
	s_add_i32 s11, s11, s86
	s_add_i32 s6, s6, s2
	s_cmpk_gt_i32 s11, 0x7ff
	s_cbranch_scc0 .LBB0_556

.LBB0_1291:
	s_ashr_i32 s7, s6, 31
	s_lshl_b64 s[0:1], s[6:7], 12
	s_ashr_i32 s7, s12, 7
	s_mul_hi_i32 s8, s7, 0xc000
	s_mul_i32 s7, s7, 0xc000
	s_add_u32 s7, s2, s7
	s_addc_u32 s13, s3, s8
	s_add_u32 s8, s7, 0x6000
	s_addc_u32 s9, s13, 0
	s_add_u32 s14, s7, 0x8000
	s_addc_u32 s15, s13, 0
	global_load_dwordx4 v[70:73], v108, s[14:15]
	global_load_dwordx4 v[74:77], v108, s[14:15] offset:16
	global_load_dwordx4 v[78:81], v109, s[14:15]
	global_load_dwordx4 v[82:85], v109, s[14:15] offset:16
	global_load_dwordx4 v[90:93], v110, s[14:15] offset:16
	global_load_dwordx4 v[86:89], v110, s[14:15]
	global_load_dwordx4 v[34:37], v108, s[8:9]
	global_load_dwordx4 v[38:41], v108, s[8:9] offset:16
	global_load_dwordx4 v[98:101], v111, s[14:15] offset:16
	global_load_dwordx4 v[94:97], v111, s[14:15]
	global_load_dwordx4 v[42:45], v109, s[8:9]
	global_load_dwordx4 v[46:49], v109, s[8:9] offset:16
	global_load_dwordx4 v[50:53], v110, s[8:9]
	global_load_dwordx4 v[54:57], v110, s[8:9] offset:16
	global_load_dwordx4 v[58:61], v111, s[8:9]
	global_load_dwordx4 v[62:65], v111, s[8:9] offset:16
	v_lshl_add_u64 v[68:69], v[66:67], 0, s[0:1]
	s_mov_b64 s[8:9], 0
	s_waitcnt vmcnt(0)
	v_pk_add_f32 v[70:71], v[70:71], 1.0 op_sel_hi:[1,0]
	v_pk_add_f32 v[72:73], v[72:73], 1.0 op_sel_hi:[1,0]
	v_pk_add_f32 v[74:75], v[74:75], 1.0 op_sel_hi:[1,0]
	v_pk_add_f32 v[76:77], v[76:77], 1.0 op_sel_hi:[1,0]
	v_pk_add_f32 v[78:79], v[78:79], 1.0 op_sel_hi:[1,0]
	v_pk_add_f32 v[80:81], v[80:81], 1.0 op_sel_hi:[1,0]
	v_pk_add_f32 v[82:83], v[82:83], 1.0 op_sel_hi:[1,0]
	v_pk_add_f32 v[84:85], v[84:85], 1.0 op_sel_hi:[1,0]
	v_pk_add_f32 v[86:87], v[86:87], 1.0 op_sel_hi:[1,0]
	v_pk_add_f32 v[88:89], v[88:89], 1.0 op_sel_hi:[1,0]
	v_pk_add_f32 v[90:91], v[90:91], 1.0 op_sel_hi:[1,0]
	v_pk_add_f32 v[92:93], v[92:93], 1.0 op_sel_hi:[1,0]
	v_pk_add_f32 v[94:95], v[94:95], 1.0 op_sel_hi:[1,0]
	v_pk_add_f32 v[96:97], v[96:97], 1.0 op_sel_hi:[1,0]
	v_pk_add_f32 v[98:99], v[98:99], 1.0 op_sel_hi:[1,0]
	v_pk_add_f32 v[100:101], v[100:101], 1.0 op_sel_hi:[1,0]
	v_lshl_add_u64 v[246:247], v[68:69], 0, s[8:9]
	v_add_co_u32_e32 v246, vcc, 0x16400000, v246
	s_nop 1
	v_addc_co_u32_e32 v247, vcc, 0, v247, vcc
	global_load_dwordx4 v[230:233], v[246:247], off offset:3072
	global_load_dwordx4 v[234:237], v[246:247], off
	global_load_dwordx4 v[238:241], v[246:247], off offset:1024
	global_load_dwordx4 v[242:245], v[246:247], off offset:2048
	s_waitcnt vmcnt(0)
	s_branch .Lnbody_LBB0_1292

.Lnbody_LBB0_1292:
	v_lshl_add_u64 v[114:115], v[68:69], 0, s[8:9]
	v_add_co_u32_e32 v126, vcc, 0x16400000, v114
	v_add_co_u32_e64 v130, s[0:1], s11, v114
	s_nop 0
	v_addc_co_u32_e32 v127, vcc, 0, v115, vcc
	v_addc_co_u32_e64 v131, s[0:1], 0, v115, s[0:1]
	s_nop 0
	s_add_u32 s8, s8, 0x1000
	s_addc_u32 s9, s9, 0
	s_cmp_eq_u32 s8, 0x10000
	v_mov_b64_e32 v[114:115], v[230:231]
	v_mov_b64_e32 v[116:117], v[232:233]
	v_mov_b64_e32 v[118:119], v[234:235]
	v_mov_b64_e32 v[120:121], v[236:237]
	v_mov_b64_e32 v[122:123], v[238:239]
	v_mov_b64_e32 v[124:125], v[240:241]
	v_mov_b64_e32 v[126:127], v[242:243]
	v_mov_b64_e32 v[128:129], v[244:245]
	s_cbranch_scc1 .Lnpf_LBB0_1292
	v_lshl_add_u64 v[246:247], v[68:69], 0, s[8:9]
	v_add_co_u32_e32 v246, vcc, 0x16400000, v246
	s_nop 1
	v_addc_co_u32_e32 v247, vcc, 0, v247, vcc
	global_load_dwordx4 v[230:233], v[246:247], off offset:3072
	global_load_dwordx4 v[234:237], v[246:247], off
	global_load_dwordx4 v[238:241], v[246:247], off offset:1024
	global_load_dwordx4 v[242:245], v[246:247], off offset:2048
.Lnpf_LBB0_1292:
	v_and_b32_e32 v135, 0xffff0000, v114
	v_and_b32_e32 v134, 0xffff0000, v116
	v_lshlrev_b32_e32 v138, 16, v120
	v_and_b32_e32 v139, 0xffff0000, v120
	v_lshlrev_b32_e32 v140, 16, v118
	v_and_b32_e32 v141, 0xffff0000, v118
	v_lshlrev_b32_e32 v133, 16, v114
	v_lshlrev_b32_e32 v132, 16, v116
	v_lshlrev_b32_e32 v136, 16, v117
	v_and_b32_e32 v114, 0xffff0000, v117
	v_lshlrev_b32_e32 v116, 16, v121
	v_and_b32_e32 v117, 0xffff0000, v121
	v_lshlrev_b32_e32 v120, 16, v119
	v_and_b32_e32 v121, 0xffff0000, v119
	v_lshlrev_b32_e32 v118, 16, v125
	v_and_b32_e32 v119, 0xffff0000, v125
	v_lshlrev_b32_e32 v142, 16, v124
	v_and_b32_e32 v143, 0xffff0000, v124
	v_lshlrev_b32_e32 v124, 16, v123
	v_and_b32_e32 v125, 0xffff0000, v123
	v_lshlrev_b32_e32 v144, 16, v122
	v_and_b32_e32 v145, 0xffff0000, v122
	v_lshlrev_b32_e32 v122, 16, v129
	v_and_b32_e32 v123, 0xffff0000, v129
	v_lshlrev_b32_e32 v146, 16, v128
	v_and_b32_e32 v147, 0xffff0000, v128
	v_lshlrev_b32_e32 v128, 16, v127
	v_and_b32_e32 v129, 0xffff0000, v127
	v_lshlrev_b32_e32 v148, 16, v126
	v_and_b32_e32 v149, 0xffff0000, v126
	v_pk_mul_f32 v[126:127], v[134:135], v[134:135]
	v_pk_mul_f32 v[152:153], v[138:139], v[138:139]
	v_pk_mul_f32 v[156:157], v[140:141], v[140:141]
	v_lshlrev_b32_e32 v137, 16, v115
	v_pk_mul_f32 v[150:151], v[116:117], v[116:117]
	v_pk_mul_f32 v[154:155], v[120:121], v[120:121]
	v_pk_mul_f32 v[164:165], v[144:145], v[144:145]
	v_mov_b32_e32 v175, v135
	v_pk_fma_f32 v[126:127], v[132:133], v[132:133], v[126:127]
	v_add_f32_e32 v113, v152, v153
	v_add_f32_e32 v135, v156, v157
	v_and_b32_e32 v115, 0xffff0000, v115
	v_pk_mul_f32 v[160:161], v[142:143], v[142:143]
	v_pk_mul_f32 v[162:163], v[124:125], v[124:125]
	v_mov_b32_e32 v174, v133
	v_add_f32_e32 v152, v164, v165
	v_mov_b32_e32 v133, v134
	v_pk_fma_f32 v[126:127], v[136:137], v[136:137], v[126:127]
	v_add_f32_e32 v113, v150, v113
	v_add_f32_e32 v134, v154, v135
	v_pk_mul_f32 v[158:159], v[118:119], v[118:119]
	v_pk_mul_f32 v[172:173], v[148:149], v[148:149]
	v_mov_b32_e32 v176, v137
	v_mov_b32_e32 v177, v115
	v_add_f32_e32 v153, v160, v161
	v_add_f32_e32 v135, v162, v152
	v_mov_b32_e32 v137, v114
	v_pk_fma_f32 v[114:115], v[114:115], v[114:115], v[126:127]
	v_add_f32_e32 v113, v151, v113
	v_add_f32_e32 v126, v155, v134
	v_pk_mul_f32 v[168:169], v[146:147], v[146:147]
	v_pk_mul_f32 v[170:171], v[128:129], v[128:129]
	v_add_f32_e32 v156, v172, v173
	v_add_f32_e32 v150, v158, v153
	v_add_f32_e32 v127, v163, v135
	v_add_f32_e32 v113, v126, v113
	v_pk_mul_f32 v[166:167], v[122:123], v[122:123]
	v_add_f32_e32 v157, v168, v169
	v_add_f32_e32 v152, v170, v156
	v_add_f32_e32 v134, v159, v150
	v_add_f32_e32 v113, v113, v127
	v_add_f32_e32 v153, v166, v157
	v_add_f32_e32 v135, v171, v152
	v_add_f32_e32 v113, v134, v113
	v_add_f32_e32 v150, v167, v153
	v_add_f32_e32 v113, v135, v113
	v_add_f32_e32 v113, v150, v113
	v_add_f32_e32 v113, v115, v113
	v_add_f32_e32 v113, v114, v113
	ds_bpermute_b32 v114, v102, v113
	s_waitcnt lgkmcnt(0)
	v_add_f32_e32 v113, v113, v114
	ds_bpermute_b32 v114, v103, v113
	s_waitcnt lgkmcnt(0)
	v_add_f32_e32 v113, v113, v114
	ds_bpermute_b32 v114, v104, v113
	s_waitcnt lgkmcnt(0)
	v_add_f32_e32 v113, v113, v114
	ds_bpermute_b32 v114, v105, v113
	s_waitcnt lgkmcnt(0)
	v_add_f32_e32 v113, v113, v114
	ds_bpermute_b32 v114, v106, v113
	s_waitcnt lgkmcnt(0)
	v_add_f32_e32 v113, v113, v114
	ds_bpermute_b32 v114, v107, v113
	s_waitcnt lgkmcnt(0)
	v_add_f32_e32 v113, v113, v114
	v_fmamk_f32 v113, v113, 0x3a000000, v112
	v_rsq_f32_e32 v114, v113
	s_nop 0
	v_pk_mul_f32 v[126:127], v[114:115], v[140:141] op_sel_hi:[0,1]
	v_pk_mul_f32 v[120:121], v[114:115], v[120:121] op_sel_hi:[0,1]
	v_pk_mul_f32 v[134:135], v[114:115], v[138:139] op_sel_hi:[0,1]
	v_pk_mul_f32 v[116:117], v[114:115], v[116:117] op_sel_hi:[0,1]
	v_pk_mul_f32 v[138:139], v[114:115], v[144:145] op_sel_hi:[0,1]
	v_pk_mul_f32 v[124:125], v[114:115], v[124:125] op_sel_hi:[0,1]
	v_pk_mul_f32 v[140:141], v[114:115], v[142:143] op_sel_hi:[0,1]
	v_pk_mul_f32 v[118:119], v[114:115], v[118:119] op_sel_hi:[0,1]
	v_pk_mul_f32 v[142:143], v[114:115], v[148:149] op_sel_hi:[0,1]
	v_pk_mul_f32 v[128:129], v[114:115], v[128:129] op_sel_hi:[0,1]
	v_pk_mul_f32 v[144:145], v[114:115], v[146:147] op_sel_hi:[0,1]
	v_pk_mul_f32 v[122:123], v[114:115], v[122:123] op_sel_hi:[0,1]
	v_pk_mul_f32 v[146:147], v[114:115], v[174:175] op_sel_hi:[0,1]
	v_pk_mul_f32 v[148:149], v[114:115], v[176:177] op_sel_hi:[0,1]
	v_pk_mul_f32 v[132:133], v[114:115], v[132:133] op_sel_hi:[0,1]
	v_pk_mul_f32 v[114:115], v[114:115], v[136:137] op_sel_hi:[0,1]
	v_pk_mul_f32 v[126:127], v[26:27], v[126:127]
	v_pk_mul_f32 v[120:121], v[28:29], v[120:121]
	v_pk_mul_f32 v[134:135], v[30:31], v[134:135]
	v_pk_mul_f32 v[116:117], v[32:33], v[116:117]
	v_pk_mul_f32 v[136:137], v[18:19], v[138:139]
	v_pk_mul_f32 v[124:125], v[20:21], v[124:125]
	v_pk_mul_f32 v[138:139], v[22:23], v[140:141]
	v_pk_mul_f32 v[118:119], v[24:25], v[118:119]
	v_pk_mul_f32 v[140:141], v[10:11], v[142:143]
	v_pk_mul_f32 v[128:129], v[12:13], v[128:129]
	v_pk_mul_f32 v[142:143], v[14:15], v[144:145]
	v_pk_mul_f32 v[122:123], v[16:17], v[122:123]
	v_pk_mul_f32 v[144:145], v[2:3], v[146:147]
	v_pk_mul_f32 v[146:147], v[4:5], v[148:149]
	v_pk_mul_f32 v[132:133], v[6:7], v[132:133]
	v_pk_mul_f32 v[114:115], v[8:9], v[114:115]
	v_pk_fma_f32 v[126:127], v[70:71], v[126:127], v[34:35]
	v_pk_fma_f32 v[120:121], v[72:73], v[120:121], v[36:37]
	v_pk_fma_f32 v[134:135], v[74:75], v[134:135], v[38:39]
	v_pk_fma_f32 v[148:149], v[76:77], v[116:117], v[40:41]
	v_pk_fma_f32 v[136:137], v[78:79], v[136:137], v[42:43]
	v_pk_fma_f32 v[124:125], v[80:81], v[124:125], v[44:45]
	v_pk_fma_f32 v[138:139], v[82:83], v[138:139], v[46:47]
	v_pk_fma_f32 v[150:151], v[84:85], v[118:119], v[48:49]
	v_pk_fma_f32 v[140:141], v[86:87], v[140:141], v[50:51]
	v_pk_fma_f32 v[128:129], v[88:89], v[128:129], v[52:53]
	v_pk_fma_f32 v[142:143], v[90:91], v[142:143], v[54:55]
	v_pk_fma_f32 v[152:153], v[92:93], v[122:123], v[56:57]
	v_pk_fma_f32 v[144:145], v[94:95], v[144:145], v[58:59]
	v_pk_fma_f32 v[146:147], v[96:97], v[146:147], v[60:61]
	v_pk_fma_f32 v[132:133], v[98:99], v[132:133], v[62:63]
	v_pk_fma_f32 v[154:155], v[100:101], v[114:115], v[64:65]
	v_cvt_pk_bf16_f32 v114, v126, v127
	v_cvt_pk_bf16_f32 v115, v120, v121
	v_cvt_pk_bf16_f32 v116, v134, v135
	v_cvt_pk_bf16_f32 v117, v148, v149
	v_cvt_pk_bf16_f32 v118, v136, v137
	v_cvt_pk_bf16_f32 v119, v124, v125
	v_cvt_pk_bf16_f32 v120, v138, v139
	v_cvt_pk_bf16_f32 v121, v150, v151
	v_cvt_pk_bf16_f32 v122, v140, v141
	v_cvt_pk_bf16_f32 v123, v128, v129
	v_cvt_pk_bf16_f32 v124, v142, v143
	v_cvt_pk_bf16_f32 v125, v152, v153
	v_cvt_pk_bf16_f32 v126, v144, v145
	v_cvt_pk_bf16_f32 v127, v146, v147
	v_cvt_pk_bf16_f32 v128, v132, v133
	v_cvt_pk_bf16_f32 v129, v154, v155
	global_store_dwordx4 v[130:131], v[114:117], off
	global_store_dwordx4 v[130:131], v[118:121], off offset:1024
	global_store_dwordx4 v[130:131], v[122:125], off offset:2048
	global_store_dwordx4 v[130:131], v[126:129], off offset:3072
	s_cbranch_scc0 .LBB0_1292
	s_add_i32 s12, s12, s86
	s_add_i32 s6, s6, s10
	s_cmpk_gt_i32 s12, 0x7ff
	s_cbranch_scc0 .LBB0_1291
